# hot item loop copy: bf16 rounding sequences fused and the post-flag-store wait removed
# baseline (speedup 1.0000x reference)
; __device__ __forceinline__ void gdn_local_item(const Params& P, LAS unsigned char* lds, int item, int tid, bool defer, int& pend, unsigned& pend_fb) {
;     ...
;         for (int r = 0; r < 7; ++r) {
;             const int id = tid + 512 * r;
;             const int row = id / 48, rem = id - row * 48, part = rem >> 4, ck = rem & 15, s = n * 64 + row - 3;
;             pr[r] = (v4u){0u, 0u, 0u, 0u};
;             if (id < 67 * 48 && s >= 0) pr[r] = *(const v4u*)(QKV + (size_t)(b * SEQ + s) * 1536 + part * 512 + h * 128 + ck * 8);
; __global__ void __launch_bounds__(NWAVES * 64, 2) hybrid_fwd(Params P) {
;     ...
;               if (NWK == 224) {
;                   for (int r = 0; r < 3; ++r) { const int q = 224 * r + wk; gdn_local_item(P, lds, (q & 7) * 128 + (q >> 3), tid, r > 0, pend, pend_fb); }
;                   if (wk < 192) { const int q = 672 + wk; gdn_local_item(P, lds, (q & 7) * 128 + (q >> 3), tid, true, pend, pend_fb); }
;                   if (wk < 160) { const int q = 864 + wk; gdn_local_item(P, lds, (q & 7) * 128 + (q >> 3), tid, true, pend, pend_fb); }
.LBB0_517:
	v_ashrrev_i32_e32 v92, 3, v91
	v_and_b32_e32 v46, 7, v91
	s_movk_i32 s0, 0x300
	v_lshlrev_b32_e32 v51, 6, v46
	v_lshlrev_b32_e32 v52, 5, v46
	s_nop 0
	s_mul_i32 s98, s58, 0xe0
	v_readlane_b32 s99, v255, 10
	s_add_i32 s98, s98, s99
	s_addk_i32 s98, 0xe0
	s_cmp_eq_u32 s58, 3
	s_cselect_b32 s99, 32, 0
	s_sub_i32 s98, s98, s99
	s_lshr_b32 s99, s98, 3
	s_cmpk_gt_u32 s99, 0x7f
	s_cbranch_scc1 .Lpf_skipA
	s_and_b32 s98, s98, 7
	s_lshr_b32 s100, s98, 2
	s_and_b32 s98, s98, 3
	s_lshl_b32 s100, s100, 13
	s_lshl_b32 s99, s99, 6
	s_add_i32 s99, s99, s100
	s_add_i32 s99, s99, -3
	s_mul_i32 s99, s99, 0xc00
	s_lshl_b32 s98, s98, 8
	s_add_u32 s98, s99, s98
	s_add_u32 s100, s24, 0x3c00000
	s_addc_u32 s101, s25, 0
	s_add_u32 s100, s100, s98
	s_addc_u32 s101, s101, 0
	s_mov_b32 s98, 0x2aaaaaab
	v_mul_hi_u32 v250, v0, s98
	v_mul_u32_u24_e32 v251, 6, v250
	v_sub_u32_e32 v251, v0, v251
	v_lshrrev_b32_e32 v252, 1, v251
	v_and_b32_e32 v251, 1, v251
	v_mul_u32_u24_e32 v250, 0xc00, v250
	v_lshl_add_u32 v250, v252, 10, v250
	v_lshl_add_u32 v250, v251, 7, v250
	v_mov_b32_e32 v251, 0x192
	v_cmp_gt_u32_e64 s[98:99], v251, v0
	s_mov_b64 exec, s[98:99]
	global_load_dword v253, v250, s[100:101]
	s_mov_b64 exec, -1
